# baseline (speedup 1.0000x reference)
.LBB1_117:
	s_cmp_lt_u32 s37, 10
	s_cselect_b32 s12, 2, -10
	s_add_i32 s12, s12, s37
	s_lshl_b32 s13, s12, 7
	s_add_u32 s14, s13, s52
	s_addc_u32 s15, 0, s53
	s_lshl_b32 s12, s12, 8
	s_add_u32 s12, s8, s12
	s_addc_u32 s13, s9, 0
	s_and_b32 s38, s36, 0x10000
	s_xor_b32 s39, s38, 0x10000
	v_or_b32_e32 v210, s38, v237
	v_mov_b32_e32 v194, v202
	v_add_u32_e32 v196, s39, v239
	v_add_u32_e32 v197, s39, v240
	v_add_u32_e32 v216, s39, v241
	v_add_u32_e32 v217, s39, v242
	v_or_b32_e32 v218, s38, v238
	v_add_u32_e32 v220, v210, v236
	ds_read_b128 v[186:189], v218 offset:32768
	ds_read_b128 v[190:193], v218 offset:34816
	ds_read_b128 v[182:185], v218 offset:36864
	ds_read_b128 v[178:181], v218 offset:38912
	ds_read_b128 v[244:247], v220
	ds_read_b128 v[248:251], v220 offset:2048
	ds_read_b128 v[252:255], v220 offset:4096
	ds_read_b128 v[210:213], v220 offset:6144
	s_waitcnt lgkmcnt(3)
	v_mfma_f32_16x16x32_f16 v[170:173], v[244:247], v[186:189], v[170:173]
	v_mfma_f32_16x16x32_f16 v[162:165], v[244:247], v[190:193], v[162:165]
	v_mfma_f32_16x16x32_f16 v[174:177], v[244:247], v[182:185], v[174:177]
	v_mfma_f32_16x16x32_f16 v[166:169], v[244:247], v[178:181], v[166:169]
	ds_read_b128 v[244:247], v220 offset:8192
	s_waitcnt vmcnt(8)
	ds_write_b128 v196, v[2:5]
	global_load_dwordx4 v[2:5], v198, s[14:15]
	s_waitcnt lgkmcnt(4)
	v_mfma_f32_16x16x32_f16 v[154:157], v[248:251], v[186:189], v[154:157]
	v_mfma_f32_16x16x32_f16 v[146:149], v[248:251], v[190:193], v[146:149]
	v_mfma_f32_16x16x32_f16 v[158:161], v[248:251], v[182:185], v[158:161]
	v_mfma_f32_16x16x32_f16 v[150:153], v[248:251], v[178:181], v[150:153]
	ds_read_b128 v[248:251], v220 offset:10240
	ds_write_b128 v197, v[6:9]
	global_load_dwordx4 v[6:9], v199, s[14:15]
	s_waitcnt lgkmcnt(5)
	v_mfma_f32_16x16x32_f16 v[138:141], v[252:255], v[186:189], v[138:141]
	v_mfma_f32_16x16x32_f16 v[130:133], v[252:255], v[190:193], v[130:133]
	v_mfma_f32_16x16x32_f16 v[142:145], v[252:255], v[182:185], v[142:145]
	v_mfma_f32_16x16x32_f16 v[134:137], v[252:255], v[178:181], v[134:137]
	ds_read_b128 v[252:255], v220 offset:12288
	ds_write_b128 v196, v[10:13] offset:2048
	global_load_dwordx4 v[10:13], v200, s[14:15]
	s_waitcnt lgkmcnt(6)
	v_mfma_f32_16x16x32_f16 v[122:125], v[210:213], v[186:189], v[122:125]
	v_mfma_f32_16x16x32_f16 v[114:117], v[210:213], v[190:193], v[114:117]
	v_mfma_f32_16x16x32_f16 v[126:129], v[210:213], v[182:185], v[126:129]
	v_mfma_f32_16x16x32_f16 v[118:121], v[210:213], v[178:181], v[118:121]
	ds_read_b128 v[210:213], v220 offset:14336
	ds_write_b128 v197, v[14:17] offset:2048
	global_load_dwordx4 v[14:17], v201, s[14:15]
	s_waitcnt lgkmcnt(7)
	v_mfma_f32_16x16x32_f16 v[106:109], v[244:247], v[186:189], v[106:109]
	v_lshl_add_u64 v[196:197], s[12:13], 0, v[194:195]
	v_mfma_f32_16x16x32_f16 v[98:101], v[244:247], v[190:193], v[98:101]
	v_mfma_f32_16x16x32_f16 v[110:113], v[244:247], v[182:185], v[110:113]
	v_mfma_f32_16x16x32_f16 v[102:105], v[244:247], v[178:181], v[102:105]
	ds_read_b128 v[244:247], v220 offset:1024
	s_waitcnt vmcnt(11)
	v_cvt_pk_f16_f32 v25, v24, v25
	v_cvt_pk_f16_f32 v24, v22, v23
	ds_write_b64 v216, v[24:25]
	global_load_dwordx4 v[22:25], v194, s[12:13] nt
	s_waitcnt lgkmcnt(7)
	v_mfma_f32_16x16x32_f16 v[90:93], v[248:251], v[186:189], v[90:93]
	v_mfma_f32_16x16x32_f16 v[82:85], v[248:251], v[190:193], v[82:85]
	v_mfma_f32_16x16x32_f16 v[94:97], v[248:251], v[182:185], v[94:97]
	v_mfma_f32_16x16x32_f16 v[86:89], v[248:251], v[178:181], v[86:89]
	ds_read_b128 v[248:251], v220 offset:3072
	s_waitcnt vmcnt(11)
	v_cvt_pk_f16_f32 v21, v20, v21
	v_cvt_pk_f16_f32 v20, v18, v19
	ds_write_b64 v216, v[20:21] offset:1024
	global_load_dwordx4 v[18:21], v194, s[12:13] offset:128 nt
	s_waitcnt lgkmcnt(7)
	v_mfma_f32_16x16x32_f16 v[74:77], v[252:255], v[186:189], v[74:77]
	v_add_co_u32_e32 v214, vcc, s23, v196
	v_mfma_f32_16x16x32_f16 v[66:69], v[252:255], v[190:193], v[66:69]
	s_nop 0
	v_addc_co_u32_e32 v215, vcc, 0, v197, vcc
	v_mfma_f32_16x16x32_f16 v[78:81], v[252:255], v[182:185], v[78:81]
	v_mfma_f32_16x16x32_f16 v[70:73], v[252:255], v[178:181], v[70:73]
	ds_read_b128 v[252:255], v220 offset:5120
	s_waitcnt vmcnt(11)
	v_cvt_pk_f16_f32 v33, v32, v33
	v_cvt_pk_f16_f32 v32, v30, v31
	ds_write_b64 v217, v[32:33]
	global_load_dwordx4 v[30:33], v[214:215], off nt
	s_waitcnt lgkmcnt(7)
	v_mfma_f32_16x16x32_f16 v[62:65], v[210:213], v[186:189], v[62:65]
	ds_read_b128 v[186:189], v220 offset:7168
	s_waitcnt vmcnt(11)
	v_mfma_f32_16x16x32_f16 v[58:61], v[210:213], v[182:185], v[58:61]
	v_cvt_pk_f16_f32 v183, v28, v29
	v_cvt_pk_f16_f32 v182, v26, v27
	global_load_dwordx4 v[26:29], v[214:215], off offset:128 nt
	v_mfma_f32_16x16x32_f16 v[54:57], v[210:213], v[190:193], v[54:57]
	ds_write_b64 v217, v[182:183] offset:1024
	v_mfma_f32_16x16x32_f16 v[50:53], v[210:213], v[178:181], v[50:53]
	ds_read_b128 v[178:181], v218 offset:33792
	ds_read_b128 v[182:185], v218 offset:35840
	ds_read_b128 v[190:193], v218 offset:37888
	ds_read_b128 v[210:213], v218 offset:39936
	s_waitcnt lgkmcnt(0)
	v_mfma_f32_16x16x32_f16 v[170:173], v[244:247], v[178:181], v[170:173]
	v_add_co_u32_e32 v214, vcc, s24, v196
	v_mfma_f32_16x16x32_f16 v[162:165], v[244:247], v[182:185], v[162:165]
	v_addc_co_u32_e32 v215, vcc, 0, v197, vcc
	v_mfma_f32_16x16x32_f16 v[174:177], v[244:247], v[190:193], v[174:177]
	v_mfma_f32_16x16x32_f16 v[166:169], v[244:247], v[210:213], v[166:169]
	ds_read_b128 v[244:247], v220 offset:9216
	s_waitcnt vmcnt(11)
	v_cvt_pk_f16_f32 v41, v40, v41
	v_cvt_pk_f16_f32 v40, v38, v39
	ds_write_b64 v216, v[40:41] offset:2048
	global_load_dwordx4 v[38:41], v[214:215], off nt
	v_mfma_f32_16x16x32_f16 v[154:157], v[248:251], v[178:181], v[154:157]
	v_mfma_f32_16x16x32_f16 v[146:149], v[248:251], v[182:185], v[146:149]
	v_mfma_f32_16x16x32_f16 v[158:161], v[248:251], v[190:193], v[158:161]
	v_mfma_f32_16x16x32_f16 v[150:153], v[248:251], v[210:213], v[150:153]
	ds_read_b128 v[248:251], v220 offset:11264
	s_waitcnt vmcnt(11)
	v_cvt_pk_f16_f32 v37, v36, v37
	v_cvt_pk_f16_f32 v36, v34, v35
	ds_write_b64 v216, v[36:37] offset:3072
	global_load_dwordx4 v[34:37], v[214:215], off offset:128 nt
	v_mfma_f32_16x16x32_f16 v[138:141], v[252:255], v[178:181], v[138:141]
	v_add_co_u32_e32 v196, vcc, s25, v196
	v_mfma_f32_16x16x32_f16 v[130:133], v[252:255], v[182:185], v[130:133]
	s_nop 0
	v_addc_co_u32_e32 v197, vcc, 0, v197, vcc
	v_mfma_f32_16x16x32_f16 v[142:145], v[252:255], v[190:193], v[142:145]
	v_mfma_f32_16x16x32_f16 v[134:137], v[252:255], v[210:213], v[134:137]
	ds_read_b128 v[252:255], v220 offset:13312
	s_waitcnt vmcnt(11)
	v_cvt_pk_f16_f32 v49, v48, v49
	v_cvt_pk_f16_f32 v48, v46, v47
	ds_write_b64 v217, v[48:49] offset:2048
	global_load_dwordx4 v[46:49], v[196:197], off nt
	v_mfma_f32_16x16x32_f16 v[122:125], v[186:189], v[178:181], v[122:125]
	v_mfma_f32_16x16x32_f16 v[114:117], v[186:189], v[182:185], v[114:117]
	v_mfma_f32_16x16x32_f16 v[126:129], v[186:189], v[190:193], v[126:129]
	v_mfma_f32_16x16x32_f16 v[118:121], v[186:189], v[210:213], v[118:121]
	ds_read_b128 v[186:189], v220 offset:15360
	s_waitcnt vmcnt(11)
	v_cvt_pk_f16_f32 v45, v44, v45
	v_cvt_pk_f16_f32 v44, v42, v43
	ds_write_b64 v217, v[44:45] offset:3072
	global_load_dwordx4 v[42:45], v[196:197], off offset:128 nt
	s_waitcnt lgkmcnt(7)
	v_mfma_f32_16x16x32_f16 v[106:109], v[244:247], v[178:181], v[106:109]
	v_mfma_f32_16x16x32_f16 v[98:101], v[244:247], v[182:185], v[98:101]
	v_mfma_f32_16x16x32_f16 v[110:113], v[244:247], v[190:193], v[110:113]
	v_mfma_f32_16x16x32_f16 v[102:105], v[244:247], v[210:213], v[102:105]
	s_waitcnt lgkmcnt(5)
	v_mfma_f32_16x16x32_f16 v[90:93], v[248:251], v[178:181], v[90:93]
	v_mfma_f32_16x16x32_f16 v[82:85], v[248:251], v[182:185], v[82:85]
	v_mfma_f32_16x16x32_f16 v[94:97], v[248:251], v[190:193], v[94:97]
	v_mfma_f32_16x16x32_f16 v[86:89], v[248:251], v[210:213], v[86:89]
	s_waitcnt lgkmcnt(3)
	v_mfma_f32_16x16x32_f16 v[74:77], v[252:255], v[178:181], v[74:77]
	v_mfma_f32_16x16x32_f16 v[66:69], v[252:255], v[182:185], v[66:69]
	v_mfma_f32_16x16x32_f16 v[78:81], v[252:255], v[190:193], v[78:81]
	v_mfma_f32_16x16x32_f16 v[70:73], v[252:255], v[210:213], v[70:73]
	s_waitcnt lgkmcnt(1)
	v_mfma_f32_16x16x32_f16 v[62:65], v[186:189], v[178:181], v[62:65]
	v_mfma_f32_16x16x32_f16 v[54:57], v[186:189], v[182:185], v[54:57]
	v_mfma_f32_16x16x32_f16 v[58:61], v[186:189], v[190:193], v[58:61]
	v_mfma_f32_16x16x32_f16 v[50:53], v[186:189], v[210:213], v[50:53]
	s_add_i32 s37, s37, 1
	s_add_i32 s36, s36, 0x10000
	s_cmp_eq_u32 s36, 0xc0000
	s_waitcnt lgkmcnt(0)
	s_barrier
	s_cbranch_scc1 .LBB1_83
